# per-tile expert-id loads in MoE unit loops read with normal cache policy (the grid barrier fences already order them) instead of device-scope sc1
# speedup vs baseline: 1.0074x; 1.0074x over previous
.LBB0_1687:
	v_cndmask_b32_e64 v2, 0, 1, s[62:63]
	v_cmp_ne_u32_e64 s[38:39], 1, v2
	s_andn2_b64 vcc, exec, s[62:63]
	s_mov_b64 s[54:55], s[64:65]
	s_cbranch_vccnz .LBB0_1689
	s_ashr_i32 s53, s52, 31
	s_ashr_i32 s51, s50, 31
	s_lshl_b64 s[54:55], s[52:53], 2
	s_add_u32 s54, s20, s54
	s_addc_u32 s55, s21, s55
	v_mov_b64_e32 v[2:3], s[54:55]
	global_load_dword v1, v[2:3], off
	s_lshl_b64 s[54:55], s[50:51], 18
	s_add_u32 s100, s22, s54
	s_addc_u32 s101, s23, s55
	s_mov_b64 s[54:55], s[64:65]

.LBB0_1800:
	s_ashr_i32 s51, s50, 31
	s_lshl_b64 s[54:55], s[50:51], 2
	s_add_u32 s54, s13, s54
	s_addc_u32 s55, s14, s55
	v_mov_b64_e32 v[2:3], s[54:55]
	s_waitcnt vmcnt(0)
	global_load_dword v2, v[2:3], off
	s_mul_i32 s54, s88, 0xe0000
	s_mul_hi_i32 s51, s88, 0xe0000
	s_add_u32 s54, s15, s54
	s_addc_u32 s51, s16, s51
	s_waitcnt vmcnt(0) lgkmcnt(0)
	v_readfirstlane_b32 s55, v2
	s_mul_hi_u32 s59, s55, 0x380000
	s_mul_i32 s55, s55, 0x380000
	s_add_u32 s54, s54, s55
	s_addc_u32 s55, s51, s59
	s_andn2_b64 vcc, exec, s[42:43]
	s_cbranch_vccz .LBB0_1776

.LBB0_1832:
	s_andn2_b64 vcc, exec, s[50:51]
	s_mov_b64 s[52:53], s[60:61]
	s_cbranch_vccnz .LBB0_1834
	s_ashr_i32 s49, s48, 31
	s_ashr_i32 s47, s46, 31
	s_lshl_b64 s[52:53], s[48:49], 2
	s_add_u32 s52, s23, s52
	s_addc_u32 s53, s70, s53
	v_mov_b64_e32 v[2:3], s[52:53]
	global_load_dword v1, v[2:3], off
	s_lshl_b64 s[52:53], s[46:47], 18
	s_add_u32 s100, s20, s52
	s_addc_u32 s101, s21, s53
	s_mov_b64 s[52:53], s[60:61]

.LBB0_1933:
	s_ashr_i32 s75, s74, 31
	s_lshl_b64 s[36:37], s[74:75], 2
	s_add_u32 s36, s66, s36
	s_addc_u32 s37, s72, s37
	v_mov_b64_e32 v[2:3], s[36:37]
	s_waitcnt vmcnt(0)
	global_load_dword v2, v[2:3], off
	s_mul_i32 s36, s13, 0xe0000
	s_mul_hi_i32 s35, s13, 0xe0000
	s_add_u32 s36, s93, s36
	s_addc_u32 s35, s94, s35
	s_waitcnt vmcnt(0) lgkmcnt(0)
	v_readfirstlane_b32 s37, v2
	s_mul_hi_u32 s42, s37, 0x380000
	s_mul_i32 s37, s37, 0x380000
	s_add_u32 s36, s36, s37
	s_addc_u32 s37, s35, s42
	s_andn2_b64 vcc, exec, s[54:55]
	s_cbranch_vccz .LBB0_1922
